# grid barrier: XCD leader posts the XCD generation bump before its own acquire invalidate (on top of the pipelined P3 combine)
# speedup vs baseline: 1.0005x; 1.0005x over previous
.LBB0_104:
	s_or_b64 exec, exec, s[8:9]
	s_mov_b64 s[8:9], exec
	v_mbcnt_lo_u32_b32 v1, s8, 0
	v_mbcnt_hi_u32_b32 v1, s9, v1
	v_cmp_eq_u32_e32 vcc, 0, v1
	s_and_saveexec_b64 s[10:11], vcc
	s_cbranch_execz .LBB0_106
	s_bcnt1_i32_b64 s2, s[8:9]
	v_mov_b32_e32 v1, 0x2000
	v_mov_b32_e32 v2, s2
	global_atomic_add v1, v2, s[6:7] offset:1024
.LBB0_106:
	s_or_b64 exec, exec, s[10:11]
	buffer_inv sc1
	s_waitcnt vmcnt(0)

.LBB0_458:
	s_or_b64 exec, exec, s[4:5]
	s_mov_b64 s[4:5], exec
	v_mbcnt_lo_u32_b32 v1, s4, 0
	v_mbcnt_hi_u32_b32 v1, s5, v1
	v_cmp_eq_u32_e32 vcc, 0, v1
	s_and_saveexec_b64 s[10:11], vcc
	s_cbranch_execz .LBB0_460
	s_bcnt1_i32_b64 s2, s[4:5]
	v_mov_b32_e32 v1, 0
	v_mov_b32_e32 v2, s2
	global_atomic_add v1, v2, s[8:9]

.LBB0_1048:
	s_or_b64 exec, exec, s[6:7]
	s_mov_b64 s[6:7], exec
	v_mbcnt_lo_u32_b32 v1, s6, 0
	v_mbcnt_hi_u32_b32 v1, s7, v1
	v_cmp_eq_u32_e32 vcc, 0, v1
	s_and_saveexec_b64 s[8:9], vcc
	s_cbranch_execz .LBB0_1050
	s_bcnt1_i32_b64 s2, s[6:7]
	v_mov_b32_e32 v1, 0
	v_mov_b32_e32 v2, s2
	global_atomic_add v1, v2, s[36:37]
.LBB0_1050:
	s_or_b64 exec, exec, s[8:9]
	buffer_inv sc1
	s_waitcnt vmcnt(0)

.LBB0_1144:
	s_or_b64 exec, exec, s[2:3]
	s_mov_b64 s[2:3], exec
	v_mbcnt_lo_u32_b32 v1, s2, 0
	v_mbcnt_hi_u32_b32 v1, s3, v1
	v_cmp_eq_u32_e32 vcc, 0, v1
	s_and_saveexec_b64 s[4:5], vcc
	s_cbranch_execz .LBB0_1146
	s_bcnt1_i32_b64 s2, s[2:3]
	v_mov_b32_e32 v1, 0
	v_mov_b32_e32 v2, s2
	global_atomic_add v1, v2, s[36:37]
.LBB0_1146:
	s_or_b64 exec, exec, s[4:5]
	buffer_inv sc1
	s_waitcnt vmcnt(0)
